# static priority raise: s_setprio 1 for waves 4-7 over the DSA attention loop, reset at loop exit; on top of v26
# baseline (speedup 1.0000x reference)
.LBB0_714:
	s_cmp_ge_u32 s96, 4
	s_cbranch_scc0 .Lprio_x_a
	s_setprio 1

.LBB0_766:
	s_waitcnt vmcnt(0)
	s_setprio 0
	s_waitcnt lgkmcnt(0)
	s_barrier
	s_mov_b64 s[0:1], 0

.LBB0_1144:
	s_waitcnt vmcnt(0)
	s_setprio 0
	s_waitcnt lgkmcnt(0)
	s_barrier
	s_cbranch_execz .LBB0_798
	s_branch .LBB0_829
